# baseline (speedup 1.0000x reference)
.LBB0_32:
	s_andn2_b64 vcc, exec, s[4:5]
	s_cbranch_vccnz .LBB0_64
	s_load_dwordx4 s[12:15], s[0:1], 0x30
	s_load_dwordx4 s[16:19], s[0:1], 0x8
	s_load_dwordx2 s[24:25], s[0:1], 0x68
	s_load_dwordx2 s[26:27], s[0:1], 0x60
	v_lshrrev_b32_e32 v39, 5, v0
	v_and_b32_e32 v46, 31, v0
	v_lshlrev_b32_e32 v1, 8, v39
	v_lshl_or_b32 v9, s2, 10, v0
	s_mov_b32 s3, 0x30d40
	v_or_b32_e32 v2, v1, v46
	v_cmp_gt_i32_e64 s[8:9], s3, v9
	v_lshlrev_b32_e32 v8, 2, v2
	v_lshlrev_b32_e32 v41, 2, v46
	v_cndmask_b32_e64 v2, 0, v9, s[8:9]
	v_ashrrev_i32_e32 v3, 31, v2
	s_waitcnt lgkmcnt(0)
	v_lshl_add_u64 v[4:5], v[2:3], 2, s[16:17]
	v_lshlrev_b64 v[2:3], 5, v[2:3]
	v_add_co_u32_e32 v6, vcc, 0xc3000, v4
	v_lshl_add_u64 v[2:3], s[18:19], 0, v[2:3]
	global_load_dword v47, v8, s[12:13]
	global_load_dword v48, v8, s[12:13] offset:128
	global_load_dword v49, v41, s[14:15] offset:128
	global_load_dword v30, v41, s[14:15] offset:256
	global_load_dword v31, v41, s[14:15] offset:384
	global_load_dword v20, v41, s[14:15] offset:512
	global_load_dword v21, v41, s[14:15] offset:640
	global_load_dword v18, v41, s[14:15] offset:768
	global_load_dword v19, v41, s[14:15] offset:896
	global_load_dword v58, v41, s[14:15]
	v_addc_co_u32_e32 v7, vcc, 0, v5, vcc
	global_load_dword v71, v[4:5], off
	global_load_dword v82, v[6:7], off offset:1280
	global_load_dwordx4 v[50:53], v[2:3], off offset:16
	global_load_dwordx4 v[54:57], v[2:3], off
	v_or_b32_e32 v2, 0x100, v9
	v_cmp_gt_i32_e64 s[6:7], s3, v2
	s_mov_b32 s10, 0xc3000
	s_load_dwordx4 s[20:23], s[0:1], 0x48
	v_cndmask_b32_e64 v2, 0, v2, s[6:7]
	v_ashrrev_i32_e32 v3, 31, v2
	v_lshl_add_u64 v[4:5], v[2:3], 2, s[16:17]
	v_lshlrev_b64 v[2:3], 5, v[2:3]
	v_add_co_u32_e32 v6, vcc, s10, v4
	v_lshl_add_u64 v[2:3], s[18:19], 0, v[2:3]
	s_nop 0
	v_addc_co_u32_e32 v7, vcc, 0, v5, vcc
	global_load_dword v69, v[4:5], off
	global_load_dword v74, v[6:7], off offset:1280
	global_load_dwordx4 v[22:25], v[2:3], off offset:16
	global_load_dwordx4 v[26:29], v[2:3], off
	v_or_b32_e32 v2, 0x200, v9
	v_cmp_gt_i32_e64 s[4:5], s3, v2
	v_or_b32_e32 v1, v1, v41
	s_nop 0
	v_cndmask_b32_e64 v2, 0, v2, s[4:5]
	v_ashrrev_i32_e32 v3, 31, v2
	v_lshl_add_u64 v[4:5], v[2:3], 2, s[16:17]
	v_lshlrev_b64 v[2:3], 5, v[2:3]
	v_add_co_u32_e32 v6, vcc, s10, v4
	v_lshl_add_u64 v[2:3], s[18:19], 0, v[2:3]
	s_nop 0
	v_addc_co_u32_e32 v7, vcc, 0, v5, vcc
	global_load_dword v65, v[4:5], off
	global_load_dword v72, v[6:7], off offset:1280
	global_load_dwordx4 v[10:13], v[2:3], off offset:16
	global_load_dwordx4 v[14:17], v[2:3], off
	v_or_b32_e32 v2, 0x300, v9
	v_cmp_gt_i32_e32 vcc, s3, v2
	s_nop 1
	v_cndmask_b32_e32 v2, 0, v2, vcc
	v_ashrrev_i32_e32 v3, 31, v2
	v_lshl_add_u64 v[4:5], v[2:3], 2, s[16:17]
	v_add_co_u32_e64 v6, s[10:11], s10, v4
	v_lshlrev_b64 v[2:3], 5, v[2:3]
	s_nop 0
	v_addc_co_u32_e64 v7, s[10:11], 0, v5, s[10:11]
	global_load_dword v61, v[4:5], off
	global_load_dword v70, v[6:7], off offset:1280
	v_lshl_add_u64 v[44:45], s[18:19], 0, v[2:3]
	global_load_dword v42, v8, s[12:13] offset:256
	global_load_dword v43, v8, s[12:13] offset:384
	global_load_dword v38, v8, s[12:13] offset:512
	global_load_dword v40, v8, s[12:13] offset:640
	global_load_dword v34, v8, s[12:13] offset:768
	global_load_dword v35, v8, s[12:13] offset:896
	s_waitcnt lgkmcnt(0)
	global_load_dword v32, v1, s[20:21]
	global_load_dword v33, v1, s[20:21] offset:128
	global_load_dword v36, v41, s[22:23]
	global_load_dword v37, v41, s[22:23] offset:128
	global_load_dwordx4 v[2:5], v[44:45], off offset:16
	global_load_dwordx4 v[6:9], v[44:45], off
	v_mbcnt_lo_u32_b32 v1, -1, 0
	v_mbcnt_hi_u32_b32 v1, -1, v1
	v_and_b32_e32 v75, 64, v1
	v_xor_b32_e32 v45, 16, v1
	s_waitcnt vmcnt(33)
	v_mul_f32_e32 v41, v48, v49
	s_waitcnt vmcnt(26)
	v_fmac_f32_e32 v41, v47, v58
	v_mov_b32_e32 v44, v41
	v_add_u32_e32 v47, 64, v75
	v_cmp_lt_i32_e64 s[10:11], v45, v47
	v_mov_b32_dpp v44, v44 quad_perm:[1,0,3,2] row_mask:0xf bank_mask:0xf
	v_add_f32_e32 v41, v41, v44
	v_mov_b32_e32 v44, v41
	s_nop 1
	v_mov_b32_dpp v44, v44 quad_perm:[2,3,0,1] row_mask:0xf bank_mask:0xf
	v_add_f32_e32 v41, v41, v44
	v_mov_b32_e32 v44, v41
	s_nop 1
	v_mov_b32_dpp v44, v44 row_half_mirror row_mask:0xf bank_mask:0xf
	v_add_f32_e32 v41, v41, v44
	v_mov_b32_e32 v44, v41
	s_nop 1
	v_mov_b32_dpp v44, v44 row_mirror row_mask:0xf bank_mask:0xf
	v_add_f32_e32 v44, v41, v44
	v_cndmask_b32_e64 v41, v1, v45, s[10:11]
	v_lshlrev_b32_e32 v41, 2, v41
	s_nop 1
	v_mov_b32_dpp v45, v44 row_bcast:15 row_mask:0xa bank_mask:0xf
	v_cmp_eq_u32_e64 s[10:11], 16, v46
	v_mov_b32_e32 v46, 0x1010
	v_mad_u32_u24 v39, v39, 20, v46
	s_and_saveexec_b64 s[12:13], s[10:11]
	s_cbranch_execz .LBB0_35
	s_waitcnt lgkmcnt(0)
	v_add_f32_e32 v44, v44, v45
	ds_write_b32 v39, v44

.LBB0_49:
	s_or_b64 exec, exec, s[10:11]
	s_mov_b64 s[12:13], s[24:25]
	s_and_saveexec_b64 s[10:11], vcc
	s_cbranch_execz .LBB0_51
	s_mov_b32 s3, 0x67b23a55
	v_mul_hi_i32 v21, v70, s3
	v_lshrrev_b32_e32 v33, 31, v21
	v_ashrrev_i32_e32 v21, 5, v21
	v_mul_hi_i32 v114, v61, s3
	v_add_lshl_u32 v21, v21, v33, 2
	v_mov_b32_e32 v33, 1
	v_lshrrev_b32_e32 v115, 31, v114
	v_ashrrev_i32_e32 v114, 5, v114
	ds_add_rtn_u32 v21, v21, v33 offset:2064
	v_add_lshl_u32 v114, v114, v115, 2
	ds_add_rtn_u32 v33, v114, v33 offset:2064
.LBB0_51:
	s_or_b64 exec, exec, s[10:11]
	s_mov_b64 s[10:11], s[26:27]
	v_cmp_gt_u32_e64 s[0:1], 64, v0
	s_waitcnt lgkmcnt(0)
	s_barrier
	s_and_saveexec_b64 s[14:15], s[0:1]
	s_cbranch_execz .LBB0_54
	v_lshlrev_b32_e32 v122, 4, v0
	ds_read_b128 v[114:117], v122 offset:2064
	v_add_u32_e32 v118, -1, v1
	v_cmp_lt_i32_e64 s[0:1], v118, v75
	v_add_u32_e32 v120, -4, v1
	s_waitcnt lgkmcnt(0)
	v_add_u32_e32 v119, v115, v114
	v_cndmask_b32_e64 v118, v118, v1, s[0:1]
	v_lshlrev_b32_e32 v118, 2, v118
	v_add3_u32 v117, v119, v116, v117
	ds_bpermute_b32 v118, v118, v117
	v_add_u32_e32 v119, -2, v1
	v_cmp_lt_i32_e64 s[0:1], v119, v75
	s_nop 1
	v_cndmask_b32_e64 v119, v119, v1, s[0:1]
	v_cmp_ne_u32_e64 s[0:1], 0, v0
	v_lshlrev_b32_e32 v119, 2, v119
	s_waitcnt lgkmcnt(0)
	v_cndmask_b32_e64 v118, 0, v118, s[0:1]
	v_add_u32_e32 v118, v118, v117
	ds_bpermute_b32 v119, v119, v118
	v_cmp_lt_u32_e64 s[0:1], 1, v0
	s_waitcnt lgkmcnt(0)
	s_nop 0
	v_cndmask_b32_e64 v119, 0, v119, s[0:1]
	v_cmp_lt_i32_e64 s[0:1], v120, v75
	v_add_u32_e32 v118, v119, v118
	s_nop 0
	v_cndmask_b32_e64 v119, v120, v1, s[0:1]
	v_lshlrev_b32_e32 v119, 2, v119
	ds_bpermute_b32 v119, v119, v118
	v_add_u32_e32 v120, -8, v1
	v_cmp_lt_u32_e64 s[0:1], 3, v0
	s_waitcnt lgkmcnt(0)
	s_nop 0
	v_cndmask_b32_e64 v119, 0, v119, s[0:1]
	v_cmp_lt_i32_e64 s[0:1], v120, v75
	v_add_u32_e32 v118, v119, v118
	s_nop 0
	v_cndmask_b32_e64 v119, v120, v1, s[0:1]
	v_lshlrev_b32_e32 v119, 2, v119
	ds_bpermute_b32 v119, v119, v118
	v_cmp_lt_u32_e64 s[0:1], 7, v0
	s_waitcnt lgkmcnt(0)
	s_nop 0
	v_cndmask_b32_e64 v119, 0, v119, s[0:1]
	v_add_u32_e32 v118, v119, v118
	v_add_u32_e32 v119, -16, v1
	v_cmp_lt_i32_e64 s[0:1], v119, v75
	s_nop 1
	v_cndmask_b32_e64 v119, v119, v1, s[0:1]
	v_lshlrev_b32_e32 v119, 2, v119
	ds_bpermute_b32 v119, v119, v118
	v_cmp_lt_u32_e64 s[0:1], 15, v0
	s_waitcnt lgkmcnt(0)
	s_nop 0
	v_cndmask_b32_e64 v119, 0, v119, s[0:1]
	v_add_u32_e32 v118, v119, v118
	v_subrev_u32_e32 v119, 32, v1
	v_cmp_lt_i32_e64 s[0:1], v119, v75
	s_nop 1
	v_cndmask_b32_e64 v1, v119, v1, s[0:1]
	v_lshlrev_b32_e32 v1, 2, v1
	ds_bpermute_b32 v1, v1, v118
	v_cmp_lt_u32_e64 s[0:1], 31, v0
	s_waitcnt lgkmcnt(0)
	s_nop 0
	v_cndmask_b32_e64 v1, 0, v1, s[0:1]
	v_add_u32_e32 v1, v1, v118
	v_sub_u32_e32 v118, v1, v117
	v_add_u32_e32 v119, v118, v114
	v_add_u32_e32 v120, v119, v115
	v_add_u32_e32 v121, v120, v116
	v_cmp_eq_u32_e64 s[0:1], 63, v0
	ds_write_b128 v122, v[118:121]
	s_and_b64 exec, exec, s[0:1]
	v_mov_b32_e32 v75, 0
	ds_write_b32 v75, v1 offset:1024

.LBB0_64:
	s_endpgm
	s_nop 0
	s_nop 0
	s_nop 0
	s_nop 0
	s_nop 0
	s_nop 0
	s_nop 0
	s_nop 0
	s_nop 0
	s_nop 0
	s_nop 0
	s_nop 0
	s_nop 0
	s_nop 0
	s_nop 0
	s_nop 0
	s_nop 0
	s_nop 0
	s_nop 0
	s_nop 0
	s_nop 0
	s_nop 0
	s_nop 0
	s_nop 0
	s_nop 0
	s_nop 0
	s_nop 0
	s_nop 0
	s_nop 0
	s_nop 0
	s_endpgm

	.amdhsa_kernel _ZN12_GLOBAL__N_16k_prepEPKfPKiS1_S1_S1_S1_S1_S1_S1_S1_S1_S1_P15HIP_vector_typeIjLj4EEPiPfPDF16_S9_S9_S1_S1_S1_S8_
		.amdhsa_group_segment_fixed_size 4272
		.amdhsa_private_segment_fixed_size 0
		.amdhsa_kernarg_size 176
		.amdhsa_user_sgpr_count 2
		.amdhsa_user_sgpr_dispatch_ptr 0
		.amdhsa_user_sgpr_queue_ptr 0
		.amdhsa_user_sgpr_kernarg_segment_ptr 1
		.amdhsa_user_sgpr_dispatch_id 0
		.amdhsa_user_sgpr_kernarg_preload_length 0
		.amdhsa_user_sgpr_kernarg_preload_offset 0
		.amdhsa_user_sgpr_private_segment_size 0
		.amdhsa_uses_dynamic_stack 0
		.amdhsa_enable_private_segment 0
		.amdhsa_system_sgpr_workgroup_id_x 1
		.amdhsa_system_sgpr_workgroup_id_y 0
		.amdhsa_system_sgpr_workgroup_id_z 0
		.amdhsa_system_sgpr_workgroup_info 0
		.amdhsa_system_vgpr_workitem_id 0
		.amdhsa_next_free_vgpr 144
		.amdhsa_next_free_sgpr 28
		.amdhsa_accum_offset 144
		.amdhsa_reserve_vcc 1
		.amdhsa_float_round_mode_32 0
		.amdhsa_float_round_mode_16_64 0
		.amdhsa_float_denorm_mode_32 3
		.amdhsa_float_denorm_mode_16_64 3
		.amdhsa_dx10_clamp 1
		.amdhsa_ieee_mode 1
		.amdhsa_fp16_overflow 0
		.amdhsa_tg_split 0
		.amdhsa_exception_fp_ieee_invalid_op 0
		.amdhsa_exception_fp_denorm_src 0
		.amdhsa_exception_fp_ieee_div_zero 0
		.amdhsa_exception_fp_ieee_overflow 0
		.amdhsa_exception_fp_ieee_underflow 0
		.amdhsa_exception_fp_ieee_inexact 0
		.amdhsa_exception_int_div_zero 0
	.end_amdhsa_kernel

amdhsa.kernels:
  - .agpr_count:     0
    .args:
      - .actual_access:  read_only
        .address_space:  global
        .offset:         0
        .size:           8
        .value_kind:     global_buffer
      - .actual_access:  read_only
        .address_space:  global
        .offset:         8
        .size:           8
        .value_kind:     global_buffer
      - .actual_access:  read_only
        .address_space:  global
        .offset:         16
        .size:           8
        .value_kind:     global_buffer
      - .actual_access:  read_only
        .address_space:  global
        .offset:         24
        .size:           8
        .value_kind:     global_buffer
      - .actual_access:  read_only
        .address_space:  global
        .offset:         32
        .size:           8
        .value_kind:     global_buffer
      - .actual_access:  read_only
        .address_space:  global
        .offset:         40
        .size:           8
        .value_kind:     global_buffer
      - .actual_access:  read_only
        .address_space:  global
        .offset:         48
        .size:           8
        .value_kind:     global_buffer
      - .actual_access:  read_only
        .address_space:  global
        .offset:         56
        .size:           8
        .value_kind:     global_buffer
      - .actual_access:  read_only
        .address_space:  global
        .offset:         64
        .size:           8
        .value_kind:     global_buffer
      - .actual_access:  read_only
        .address_space:  global
        .offset:         72
        .size:           8
        .value_kind:     global_buffer
      - .actual_access:  read_only
        .address_space:  global
        .offset:         80
        .size:           8
        .value_kind:     global_buffer
      - .actual_access:  read_only
        .address_space:  global
        .offset:         88
        .size:           8
        .value_kind:     global_buffer
      - .actual_access:  write_only
        .address_space:  global
        .offset:         96
        .size:           8
        .value_kind:     global_buffer
      - .actual_access:  write_only
        .address_space:  global
        .offset:         104
        .size:           8
        .value_kind:     global_buffer
      - .actual_access:  write_only
        .address_space:  global
        .offset:         112
        .size:           8
        .value_kind:     global_buffer
      - .actual_access:  write_only
        .address_space:  global
        .offset:         120
        .size:           8
        .value_kind:     global_buffer
      - .actual_access:  write_only
        .address_space:  global
        .offset:         128
        .size:           8
        .value_kind:     global_buffer
      - .actual_access:  write_only
        .address_space:  global
        .offset:         136
        .size:           8
        .value_kind:     global_buffer
      - .actual_access:  read_only
        .address_space:  global
        .offset:         144
        .size:           8
        .value_kind:     global_buffer
      - .actual_access:  read_only
        .address_space:  global
        .offset:         152
        .size:           8
        .value_kind:     global_buffer
      - .actual_access:  read_only
        .address_space:  global
        .offset:         160
        .size:           8
        .value_kind:     global_buffer
      - .actual_access:  write_only
        .address_space:  global
        .offset:         168
        .size:           8
        .value_kind:     global_buffer
    .group_segment_fixed_size: 4272
    .kernarg_segment_align: 8
    .kernarg_segment_size: 176
    .language:       OpenCL C
    .language_version:
      - 2
      - 0
    .max_flat_workgroup_size: 256
    .name:           _ZN12_GLOBAL__N_16k_prepEPKfPKiS1_S1_S1_S1_S1_S1_S1_S1_S1_S1_P15HIP_vector_typeIjLj4EEPiPfPDF16_S9_S9_S1_S1_S1_S8_
    .private_segment_fixed_size: 0
    .sgpr_count:     34
    .sgpr_spill_count: 0
    .symbol:         _ZN12_GLOBAL__N_16k_prepEPKfPKiS1_S1_S1_S1_S1_S1_S1_S1_S1_S1_P15HIP_vector_typeIjLj4EEPiPfPDF16_S9_S9_S1_S1_S1_S8_.kd
    .uniform_work_group_size: 1
    .uses_dynamic_stack: false
    .vgpr_count:     144
    .vgpr_spill_count: 0
    .wavefront_size: 64
  - .agpr_count:     0
    .args:
      - .actual_access:  read_only
        .address_space:  global
        .offset:         0
        .size:           8
        .value_kind:     global_buffer
      - .actual_access:  read_only
        .address_space:  global
        .offset:         8
        .size:           8
        .value_kind:     global_buffer
      - .actual_access:  write_only
        .address_space:  global
        .offset:         16
        .size:           8
        .value_kind:     global_buffer
      - .actual_access:  write_only
        .address_space:  global
        .offset:         24
        .size:           8
        .value_kind:     global_buffer
      - .actual_access:  read_only
        .address_space:  global
        .offset:         32
        .size:           8
        .value_kind:     global_buffer
      - .actual_access:  read_only
        .address_space:  global
        .offset:         40
        .size:           8
        .value_kind:     global_buffer
      - .actual_access:  write_only
        .address_space:  global
        .offset:         48
        .size:           8
        .value_kind:     global_buffer
      - .actual_access:  write_only
        .address_space:  global
        .offset:         56
        .size:           8
        .value_kind:     global_buffer
      - .actual_access:  write_only
        .address_space:  global
        .offset:         64
        .size:           8
        .value_kind:     global_buffer
    .group_segment_fixed_size: 7268
    .kernarg_segment_align: 8
    .kernarg_segment_size: 72
    .language:       OpenCL C
    .language_version:
      - 2
      - 0
    .max_flat_workgroup_size: 1024
    .name:           _ZN12_GLOBAL__N_18k_bucketEPK15HIP_vector_typeIjLj4EEPKiPiPS1_PKfS9_PDF16_PfSB_
    .private_segment_fixed_size: 0
    .sgpr_count:     34
    .sgpr_spill_count: 0
    .symbol:         _ZN12_GLOBAL__N_18k_bucketEPK15HIP_vector_typeIjLj4EEPKiPiPS1_PKfS9_PDF16_PfSB_.kd
    .uniform_work_group_size: 1
    .uses_dynamic_stack: false
    .vgpr_count:     62
    .vgpr_spill_count: 0
    .wavefront_size: 64
  - .agpr_count:     0
    .args:
      - .actual_access:  read_only
        .address_space:  global
        .offset:         0
        .size:           8
        .value_kind:     global_buffer
      - .actual_access:  read_only
        .address_space:  global
        .offset:         8
        .size:           8
        .value_kind:     global_buffer
      - .actual_access:  read_only
        .address_space:  global
        .offset:         16
        .size:           8
        .value_kind:     global_buffer
      - .actual_access:  read_only
        .address_space:  global
        .offset:         24
        .size:           8
        .value_kind:     global_buffer
      - .actual_access:  read_only
        .address_space:  global
        .offset:         32
        .size:           8
        .value_kind:     global_buffer
      - .actual_access:  read_only
        .address_space:  global
        .offset:         40
        .size:           8
        .value_kind:     global_buffer
      - .actual_access:  read_only
        .address_space:  global
        .offset:         48
        .size:           8
        .value_kind:     global_buffer
      - .actual_access:  read_only
        .address_space:  global
        .offset:         56
        .size:           8
        .value_kind:     global_buffer
      - .actual_access:  read_only
        .address_space:  global
        .offset:         64
        .size:           8
        .value_kind:     global_buffer
      - .actual_access:  read_only
        .address_space:  global
        .offset:         72
        .size:           8
        .value_kind:     global_buffer
      - .actual_access:  write_only
        .address_space:  global
        .offset:         80
        .size:           8
        .value_kind:     global_buffer
      - .actual_access:  write_only
        .address_space:  global
        .offset:         88
        .size:           8
        .value_kind:     global_buffer
      - .actual_access:  write_only
        .address_space:  global
        .offset:         96
        .size:           8
        .value_kind:     global_buffer
      - .actual_access:  read_only
        .address_space:  global
        .offset:         104
        .size:           8
        .value_kind:     global_buffer
    .group_segment_fixed_size: 25216
    .kernarg_segment_align: 8
    .kernarg_segment_size: 112
    .language:       OpenCL C
    .language_version:
      - 2
      - 0
    .max_flat_workgroup_size: 256
    .name:           _ZN12_GLOBAL__N_18k_layer1EPKDF16_PKfS3_PKiPK15HIP_vector_typeIjLj4EES1_S3_S1_S3_S3_PDF16_PfSB_S3_
    .private_segment_fixed_size: 0
    .sgpr_count:     106
    .sgpr_spill_count: 0
    .symbol:         _ZN12_GLOBAL__N_18k_layer1EPKDF16_PKfS3_PKiPK15HIP_vector_typeIjLj4EES1_S3_S1_S3_S3_PDF16_PfSB_S3_.kd
    .uniform_work_group_size: 1
    .uses_dynamic_stack: false
    .vgpr_count:     96
    .vgpr_spill_count: 0
    .wavefront_size: 64
  - .agpr_count:     0
    .args:
      - .actual_access:  read_only
        .address_space:  global
        .offset:         0
        .size:           8
        .value_kind:     global_buffer
      - .actual_access:  read_only
        .address_space:  global
        .offset:         8
        .size:           8
        .value_kind:     global_buffer
      - .actual_access:  read_only
        .address_space:  global
        .offset:         16
        .size:           8
        .value_kind:     global_buffer
      - .actual_access:  read_only
        .address_space:  global
        .offset:         24
        .size:           8
        .value_kind:     global_buffer
      - .actual_access:  read_only
        .address_space:  global
        .offset:         32
        .size:           8
        .value_kind:     global_buffer
      - .actual_access:  read_only
        .address_space:  global
        .offset:         40
        .size:           8
        .value_kind:     global_buffer
      - .actual_access:  read_only
        .address_space:  global
        .offset:         48
        .size:           8
        .value_kind:     global_buffer
      - .actual_access:  write_only
        .address_space:  global
        .offset:         56
        .size:           8
        .value_kind:     global_buffer
    .group_segment_fixed_size: 6144
    .kernarg_segment_align: 8
    .kernarg_segment_size: 64
    .language:       OpenCL C
    .language_version:
      - 2
      - 0
    .max_flat_workgroup_size: 256
    .name:           _ZN12_GLOBAL__N_18k_layer2EPKDF16_PKfS3_PKiPK15HIP_vector_typeIjLj4EES3_S3_PDF16_
    .private_segment_fixed_size: 0
    .sgpr_count:     42
    .sgpr_spill_count: 0
    .symbol:         _ZN12_GLOBAL__N_18k_layer2EPKDF16_PKfS3_PKiPK15HIP_vector_typeIjLj4EES3_S3_PDF16_.kd
    .uniform_work_group_size: 1
    .uses_dynamic_stack: false
    .vgpr_count:     70
    .vgpr_spill_count: 0
    .wavefront_size: 64
  - .agpr_count:     0
    .args:
      - .actual_access:  read_only
        .address_space:  global
        .offset:         0
        .size:           8
        .value_kind:     global_buffer
      - .actual_access:  read_only
        .address_space:  global
        .offset:         8
        .size:           8
        .value_kind:     global_buffer
      - .actual_access:  read_only
        .address_space:  global
        .offset:         16
        .size:           8
        .value_kind:     global_buffer
      - .actual_access:  read_only
        .address_space:  global
        .offset:         24
        .size:           8
        .value_kind:     global_buffer
      - .actual_access:  read_only
        .address_space:  global
        .offset:         32
        .size:           8
        .value_kind:     global_buffer
      - .actual_access:  read_only
        .address_space:  global
        .offset:         40
        .size:           8
        .value_kind:     global_buffer
      - .actual_access:  write_only
        .address_space:  global
        .offset:         48
        .size:           8
        .value_kind:     global_buffer
    .group_segment_fixed_size: 16384
    .kernarg_segment_align: 8
    .kernarg_segment_size: 56
    .language:       OpenCL C
    .language_version:
      - 2
      - 0
    .max_flat_workgroup_size: 512
    .name:           _ZN12_GLOBAL__N_17k_pairsEPKDF16_PKiS1_PKfS5_S5_Pf
    .private_segment_fixed_size: 0
    .sgpr_count:     46
    .sgpr_spill_count: 0
    .symbol:         _ZN12_GLOBAL__N_17k_pairsEPKDF16_PKiS1_PKfS5_S5_Pf.kd
    .uniform_work_group_size: 1
    .uses_dynamic_stack: false
    .vgpr_count:     78
    .vgpr_spill_count: 0
    .wavefront_size: 64
